# baseline (speedup 1.0000x reference)
.LBB1_28:
	s_and_b64 vcc, exec, s[4:5]
	s_cbranch_vccz .LBB1_33
	s_load_dwordx4 s[36:39], s[0:1], 0x30
	s_sleep 16
	s_lshl_b32 s0, s2, 3
	s_addk_i32 s0, 0xfc00
	v_or_b32_e32 v1, s0, v1
	v_lshlrev_b32_e32 v1, 1, v1
	s_ashr_i32 s0, s0, 8
	v_and_b32_e32 v19, 0x1fe, v1
	v_mov_b32_e32 v1, 0
	v_lshl_or_b32 v2, s0, 12, v0
	v_mov_b32_e32 v3, v1
	s_waitcnt vmcnt(8) lgkmcnt(0)
	v_lshl_add_u64 v[4:5], v[2:3], 2, s[6:7]
	v_or_b32_e32 v6, 0x400, v2
	v_or_b32_e32 v8, 0x600, v2
	v_or_b32_e32 v10, 0x800, v2
	v_or_b32_e32 v12, 0xa00, v2
	v_or_b32_e32 v16, 0xc00, v2
	v_or_b32_e32 v2, 0xe00, v2
	s_ashr_i32 s1, s0, 31
	v_mov_b32_e32 v7, v1
	v_mov_b32_e32 v9, v1
	v_mov_b32_e32 v11, v1
	v_mov_b32_e32 v13, v1
	v_mov_b32_e32 v17, v1
	v_lshl_add_u64 v[2:3], v[2:3], 2, s[6:7]
	s_lshl_b64 s[34:35], s[0:1], 9
	v_and_b32_e32 v15, 63, v0
	v_lshl_add_u64 v[6:7], v[6:7], 2, s[6:7]
	v_lshl_add_u64 v[8:9], v[8:9], 2, s[6:7]
	v_lshl_add_u64 v[10:11], v[10:11], 2, s[6:7]
	v_lshl_add_u64 v[12:13], v[12:13], 2, s[6:7]
	v_lshl_add_u64 v[16:17], v[16:17], 2, s[6:7]
	global_load_dword v20, v[4:5], off
	global_load_dword v21, v[4:5], off offset:2048
	global_load_dword v22, v[6:7], off
	global_load_dword v23, v[8:9], off
	global_load_dword v24, v[10:11], off
	global_load_dword v25, v[12:13], off
	global_load_dword v26, v[16:17], off
	global_load_dword v27, v[2:3], off
	v_or_b32_e32 v0, s34, v19
	s_movk_i32 s33, 0xc00
	v_mov_b64_e32 v[2:3], s[36:37]
	v_mad_u64_u32 v[2:3], s[2:3], v0, s33, v[2:3]
	v_mov_b32_e32 v0, 0xc00
	v_mad_i32_i24 v3, s1, v0, v3
	v_lshlrev_b32_e32 v0, 2, v15
	v_lshl_add_u64 v[4:5], v[2:3], 0, v[0:1]
	s_movk_i32 s0, 0x1000
	v_add_co_u32_e32 v2, vcc, s0, v4
	s_nop 1
	v_addc_co_u32_e32 v3, vcc, 0, v5, vcc
	global_load_dword v18, v[4:5], off offset:3072
	global_load_dword v17, v[4:5], off offset:3328
	global_load_dword v16, v[4:5], off offset:3584
	global_load_dword v15, v[4:5], off offset:3840
	global_load_dword v13, v[2:3], off
	global_load_dword v12, v[2:3], off offset:256
	global_load_dword v11, v[2:3], off offset:512
	global_load_dword v10, v[2:3], off offset:768
	global_load_dword v9, v[2:3], off offset:1024
	global_load_dword v8, v[2:3], off offset:1280
	global_load_dword v7, v[2:3], off offset:1536
	global_load_dword v6, v[2:3], off offset:1792
	v_lshlrev_b32_e32 v2, 2, v19
	s_waitcnt vmcnt(17)
	v_max3_i32 v3, v20, v21, v22
	s_waitcnt vmcnt(15)
	v_max3_i32 v3, v3, v23, v24
	s_waitcnt vmcnt(13)
	v_max3_i32 v3, v3, v25, v26
	s_waitcnt vmcnt(12)
	v_max3_i32 v3, v3, v27, -1
	ds_write_b32 v14, v3 offset:32768
	s_waitcnt lgkmcnt(0)
	s_barrier
	ds_read_b64 v[2:3], v2 offset:32768
	ds_read2st64_b32 v[20:21], v0 offset0:128 offset1:129
	ds_read2st64_b32 v[22:23], v0 offset0:130 offset1:131
	ds_read2st64_b32 v[24:25], v0 offset0:132 offset1:133
	ds_read2st64_b32 v[26:27], v0 offset0:134 offset1:135
	s_waitcnt lgkmcnt(4)
	v_cmp_lt_i32_e64 s[30:31], -1, v2
	s_waitcnt lgkmcnt(3)
	v_cmp_eq_u32_e32 vcc, v20, v2
	v_cmp_eq_u32_e64 s[0:1], v20, v3
	v_cmp_eq_u32_e64 s[16:17], v21, v2
	v_cmp_eq_u32_e64 s[2:3], v21, v3
	s_waitcnt lgkmcnt(2)
	v_cmp_eq_u32_e64 s[18:19], v22, v2
	v_cmp_eq_u32_e64 s[4:5], v22, v3
	v_cmp_eq_u32_e64 s[20:21], v23, v2
	v_cmp_eq_u32_e64 s[6:7], v23, v3
	s_waitcnt lgkmcnt(1)
	v_cmp_eq_u32_e64 s[22:23], v24, v2
	v_cmp_eq_u32_e64 s[8:9], v24, v3
	v_cmp_eq_u32_e64 s[24:25], v25, v2
	v_cmp_eq_u32_e64 s[10:11], v25, v3
	s_waitcnt lgkmcnt(0)
	v_cmp_eq_u32_e64 s[26:27], v26, v2
	v_cmp_eq_u32_e64 s[12:13], v26, v3
	v_cmp_eq_u32_e64 s[28:29], v27, v2
	v_cmp_eq_u32_e64 s[14:15], v27, v3
	s_and_saveexec_b64 s[36:37], s[30:31]
	s_cbranch_execz .LBB1_31
	global_load_dword v14, v[4:5], off
	global_load_dword v19, v[4:5], off offset:256
	global_load_dword v22, v[4:5], off offset:512
	global_load_dword v23, v[4:5], off offset:768
	global_load_dword v24, v[4:5], off offset:1024
	global_load_dword v25, v[4:5], off offset:1280
	global_load_dword v26, v[4:5], off offset:1536
	global_load_dword v27, v[4:5], off offset:1792
	global_load_dword v28, v[4:5], off offset:2048
	global_load_dword v29, v[4:5], off offset:2304
	global_load_dword v30, v[4:5], off offset:2560
	global_load_dword v31, v[4:5], off offset:2816
	s_bcnt1_i32_b64 s30, vcc
	s_bcnt1_i32_b64 s16, s[16:17]
	s_bcnt1_i32_b64 s17, s[18:19]
	s_add_i32 s16, s30, s16
	s_bcnt1_i32_b64 s18, s[20:21]
	s_add_i32 s16, s16, s17
	s_bcnt1_i32_b64 s19, s[22:23]
	s_add_i32 s16, s16, s18
	s_bcnt1_i32_b64 s20, s[24:25]
	s_add_i32 s16, s16, s19
	s_bcnt1_i32_b64 s21, s[26:27]
	s_add_i32 s16, s16, s20
	s_bcnt1_i32_b64 s22, s[28:29]
	s_add_i32 s16, s16, s21
	s_add_i32 s16, s16, s22
	v_mov_b32_e32 v4, v2
	v_cvt_f32_u32_e32 v2, s16
	v_mov_b32_e32 v5, v1
	v_mov_b64_e32 v[20:21], s[38:39]
	v_lshl_add_u64 v[4:5], s[34:35], 0, v[4:5]
	v_div_scale_f32 v32, s[16:17], v2, v2, 1.0
	v_rcp_f32_e32 v33, v32
	v_mad_u64_u32 v[20:21], s[16:17], v4, s33, v[20:21]
	v_mad_i32_i24 v21, v5, s33, v21
	v_lshl_add_u64 v[4:5], v[20:21], 0, v[0:1]
	v_fma_f32 v20, -v32, v33, 1.0
	v_div_scale_f32 v1, vcc, 1.0, v2, 1.0
	v_fmac_f32_e32 v33, v20, v33
	v_mul_f32_e32 v20, v1, v33
	v_fma_f32 v21, -v32, v20, v1
	v_fmac_f32_e32 v20, v21, v33
	v_fma_f32 v1, -v32, v20, v1
	v_div_fmas_f32 v1, v1, v33, v20
	v_div_fixup_f32 v1, v1, v2, 1.0
	s_waitcnt vmcnt(11)
	v_mul_f32_e32 v2, v1, v14
	s_waitcnt vmcnt(10)
	v_mul_f32_e32 v14, v1, v19
	s_waitcnt vmcnt(9)
	v_mul_f32_e32 v19, v1, v22
	s_waitcnt vmcnt(8)
	v_mul_f32_e32 v20, v1, v23
	s_waitcnt vmcnt(7)
	v_mul_f32_e32 v21, v1, v24
	s_waitcnt vmcnt(6)
	v_mul_f32_e32 v22, v1, v25
	s_waitcnt vmcnt(5)
	v_mul_f32_e32 v23, v1, v26
	s_waitcnt vmcnt(4)
	v_mul_f32_e32 v24, v1, v27
	s_waitcnt vmcnt(3)
	v_mul_f32_e32 v25, v1, v28
	s_waitcnt vmcnt(2)
	v_mul_f32_e32 v26, v1, v29
	s_waitcnt vmcnt(1)
	v_mul_f32_e32 v27, v1, v30
	global_atomic_add_f32 v[4:5], v2, off
	global_atomic_add_f32 v[4:5], v14, off offset:256
	global_atomic_add_f32 v[4:5], v19, off offset:512
	global_atomic_add_f32 v[4:5], v20, off offset:768
	global_atomic_add_f32 v[4:5], v21, off offset:1024
	global_atomic_add_f32 v[4:5], v22, off offset:1280
	global_atomic_add_f32 v[4:5], v23, off offset:1536
	global_atomic_add_f32 v[4:5], v24, off offset:1792
	global_atomic_add_f32 v[4:5], v25, off offset:2048
	global_atomic_add_f32 v[4:5], v26, off offset:2304
	global_atomic_add_f32 v[4:5], v27, off offset:2560
	s_waitcnt vmcnt(11)
	v_mul_f32_e32 v1, v1, v31
	global_atomic_add_f32 v[4:5], v1, off offset:2816
